# speedup vs baseline: 1.0431x; 1.0431x over previous
.Lmask_ready:
	s_sub_u32 s26, 0x1ff, s2
	s_mul_i32 s26, s26, 9
	s_lshr_b32 s26, s26, 6
	s_min_u32 s26, s26, 96
	s_cmp_eq_u32 s26, 0
	s_cbranch_scc1 .Lhold_done
